# speedup vs baseline: 1.0676x; 1.0676x over previous
.LBB0_37:
	s_or_b64 exec, exec, s[0:1]
	v_mov_b32_e32 v98, v97
	v_mov_b32_e32 v99, v97
	v_mov_b32_e32 v5, v97
	v_mov_b32_e32 v6, v97
	v_mov_b32_e32 v7, v97
	v_mov_b32_e32 v1, v97
	v_mov_b32_e32 v2, v97
	v_mov_b32_e32 v3, v97
	s_mov_b32 s0, 0x10000
	v_or_b32_e32 v8, 0x21000, v223
	v_mfma_f32_32x32x16_f16 v[32:47], v[96:99], v[0:3], 0
	v_mfma_f32_32x32x16_f16 v[16:31], v[4:7], v[0:3], 0
	v_or_b32_e32 v114, 0x21000, v223
	v_cmp_eq_u32_e64 s[0:1], 0, v225
	s_and_b64 vcc, vcc, s[0:1]
	ds_read_b128 v[8:11], v114
	ds_read_b128 v[12:15], v114 offset:32
	ds_read_b128 v[234:237], v114 offset:64
	ds_read_b128 v[238:241], v114 offset:96
	ds_read_b128 v[242:245], v114 offset:128
	ds_read_b128 v[106:109], v114 offset:160
	ds_read_b128 v[110:113], v114 offset:192
	s_waitcnt lgkmcnt(7)
	v_mfma_f32_32x32x16_f16 v[32:47], v[180:183], v[92:95], v[32:47]
	ds_read_b128 v[0:3], v114 offset:224
	v_mfma_f32_32x32x16_f16 v[32:47], v[184:187], v[88:91], v[32:47]
	v_mfma_f32_32x32x16_f16 v[32:47], v[188:191], v[84:87], v[32:47]
	v_mfma_f32_32x32x16_f16 v[32:47], v[192:195], v[80:83], v[32:47]
	v_mfma_f32_32x32x16_f16 v[32:47], v[196:199], v[76:79], v[32:47]
	v_mfma_f32_32x32x16_f16 v[32:47], v[200:203], v[72:75], v[32:47]
	v_mfma_f32_32x32x16_f16 v[32:47], v[204:207], v[68:71], v[32:47]
	v_mfma_f32_32x32x16_f16 v[32:47], v[208:211], v[64:67], v[32:47]
	s_waitcnt lgkmcnt(0)
	v_dot2c_f32_f16_e32 v98, v92, v8
	v_mfma_f32_32x32x16_f16 v[16:31], v[148:151], v[92:95], v[16:31]
	v_dot2c_f32_f16_e32 v98, v93, v9
	v_dot2c_f32_f16_e32 v98, v94, v10
	v_dot2c_f32_f16_e32 v98, v95, v11
	v_dot2c_f32_f16_e32 v98, v88, v12
	v_mfma_f32_32x32x16_f16 v[16:31], v[152:155], v[88:91], v[16:31]
	v_dot2c_f32_f16_e32 v98, v89, v13
	v_dot2c_f32_f16_e32 v98, v90, v14
	v_dot2c_f32_f16_e32 v98, v91, v15
	v_dot2c_f32_f16_e32 v98, v84, v234
	v_mfma_f32_32x32x16_f16 v[16:31], v[156:159], v[84:87], v[16:31]
	v_dot2c_f32_f16_e32 v98, v85, v235
	v_dot2c_f32_f16_e32 v98, v86, v236
	v_dot2c_f32_f16_e32 v98, v87, v237
	v_dot2c_f32_f16_e32 v98, v80, v238
	v_mfma_f32_32x32x16_f16 v[16:31], v[160:163], v[80:83], v[16:31]
	v_dot2c_f32_f16_e32 v98, v81, v239
	v_dot2c_f32_f16_e32 v98, v82, v240
	v_dot2c_f32_f16_e32 v98, v83, v241
	v_dot2c_f32_f16_e32 v98, v76, v242
	v_mfma_f32_32x32x16_f16 v[16:31], v[164:167], v[76:79], v[16:31]
	v_dot2c_f32_f16_e32 v98, v77, v243
	v_dot2c_f32_f16_e32 v98, v78, v244
	v_dot2c_f32_f16_e32 v98, v79, v245
	v_dot2c_f32_f16_e32 v98, v72, v106
	v_mfma_f32_32x32x16_f16 v[16:31], v[168:171], v[72:75], v[16:31]
	v_dot2c_f32_f16_e32 v98, v73, v107
	v_dot2c_f32_f16_e32 v98, v74, v108
	v_dot2c_f32_f16_e32 v98, v75, v109
	v_dot2c_f32_f16_e32 v98, v68, v110
	v_mfma_f32_32x32x16_f16 v[16:31], v[172:175], v[68:71], v[16:31]
	v_dot2c_f32_f16_e32 v98, v69, v111
	v_dot2c_f32_f16_e32 v98, v70, v112
	v_dot2c_f32_f16_e32 v98, v71, v113
	v_cvt_pk_f16_f32 v7, v38, v39
	v_cvt_pk_f16_f32 v6, v36, v37
	v_cvt_pk_f16_f32 v5, v34, v35
	v_cvt_pk_f16_f32 v4, v32, v33
	v_dot2c_f32_f16_e32 v98, v64, v0
	v_dot2c_f32_f16_e32 v98, v65, v1
	v_dot2c_f32_f16_e32 v98, v66, v2
	v_mfma_f32_32x32x16_f16 v[16:31], v[176:179], v[64:67], v[16:31]
	v_dot2c_f32_f16_e32 v98, v67, v3
	v_cvt_pk_f16_f32 v35, v46, v47
	v_cvt_pk_f16_f32 v34, v44, v45
	v_cvt_pk_f16_f32 v33, v42, v43
	v_cvt_pk_f16_f32 v32, v40, v41
	ds_bpermute_b32 v36, v102, v98
	v_cvt_f32_i32_e32 v37, v226
	v_mfma_f32_32x32x16_f16 v[0:15], v[4:7], v[60:63], 0
	s_nop 3
	v_cvt_pk_f16_f32 v23, v22, v23
	v_cvt_pk_f16_f32 v22, v20, v21
	v_cvt_pk_f16_f32 v21, v18, v19
	v_cvt_pk_f16_f32 v20, v16, v17
	v_cvt_pk_f16_f32 v19, v30, v31
	v_cvt_pk_f16_f32 v18, v28, v29
	v_cvt_pk_f16_f32 v17, v26, v27
	v_mfma_f32_32x32x16_f16 v[0:15], v[32:35], v[56:59], v[0:15]
	v_cvt_pk_f16_f32 v16, v24, v25
	s_waitcnt lgkmcnt(0)
	v_add_f32_e32 v36, v98, v36
	v_cvt_f16_f32_e32 v26, v100
	v_mov_b32_e32 v98, v97
	v_lshlrev_b32_e32 v32, 6, v218
	v_mfma_f32_32x32x16_f16 v[0:15], v[20:23], v[52:55], v[0:15]
	v_fma_mixlo_f16 v20, v37, v104, v36
	v_pack_b32_f16 v20, v20, 0
	v_pack_b32_f16 v21, v26, 0
	v_cndmask_b32_e32 v96, 0, v21, vcc
	v_mfma_f32_32x32x16_f16 v[0:15], v[16:19], v[48:51], v[0:15]
	v_cndmask_b32_e32 v16, 0, v20, vcc
	v_mov_b32_e32 v17, v97
	v_mov_b32_e32 v18, v97
	v_mov_b32_e32 v19, v97
	v_cmp_ne_u32_e32 vcc, 0, v225
	s_nop 0
	v_mfma_f32_32x32x16_f16 v[0:15], v[16:19], v[96:99], v[0:15]
	v_lshlrev_b32_e32 v70, 2, v215
	v_lshl_add_u32 v70, v214, 4, v70
	global_load_dwordx4 v[16:19], v70, s[2:3]
	global_load_dwordx4 v[20:23], v70, s[2:3] offset:32
	global_load_dwordx4 v[24:27], v70, s[2:3] offset:64
	global_load_dwordx4 v[28:31], v70, s[2:3] offset:96
	s_and_saveexec_b64 s[6:7], vcc
	s_cbranch_execz .LBB0_39
	v_lshl_or_b32 v71, v222, 12, v32
	v_add_u32_e32 v71, 0x18800, v71
	s_nop 7
	ds_write_b128 v71, v[0:3]
	ds_write_b128 v71, v[4:7] offset:16
	ds_write_b128 v71, v[8:11] offset:32
	ds_write_b128 v71, v[12:15] offset:48
.LBB0_39:
	s_or_b64 exec, exec, s[6:7]
	v_cvt_pk_f16_f32 v73, v118, v119
	v_cvt_pk_f16_f32 v72, v116, v117
	v_add_u32_e32 v76, v103, v105
	v_cvt_pk_f16_f32 v75, v122, v123
	v_cvt_pk_f16_f32 v74, v120, v121
	s_waitcnt lgkmcnt(0)
	s_barrier
	ds_write2_b64 v76, v[72:73], v[74:75] offset1:34
	v_cvt_pk_f16_f32 v73, v126, v127
	v_cvt_pk_f16_f32 v72, v124, v125
	v_cvt_pk_f16_f32 v75, v130, v131
	v_cvt_pk_f16_f32 v74, v128, v129
	ds_write2_b64 v76, v[72:73], v[74:75] offset0:68 offset1:102
	v_cvt_pk_f16_f32 v73, v134, v135
	v_cvt_pk_f16_f32 v72, v132, v133
	v_cvt_pk_f16_f32 v75, v138, v139
	v_cvt_pk_f16_f32 v74, v136, v137
	ds_write2_b64 v76, v[72:73], v[74:75] offset0:136 offset1:170
	v_cvt_pk_f16_f32 v73, v142, v143
	v_cvt_pk_f16_f32 v72, v140, v141
	v_cvt_pk_f16_f32 v75, v146, v147
	v_cvt_pk_f16_f32 v74, v144, v145
	ds_write2_b64 v76, v[72:73], v[74:75] offset0:204 offset1:238
	s_and_saveexec_b64 s[6:7], s[0:1]
	s_cbranch_execz .LBB0_49
	v_mov_b32_e32 v215, 0
	v_add_u32_e32 v54, v224, v223
	ds_read_b128 v[34:37], v54
	s_movk_i32 s0, 0x110
	v_mad_u32_u24 v70, v220, s0, v223
	ds_read_b128 v[38:41], v70 offset:34816
	ds_read_b128 v[42:45], v54 offset:32
	ds_read_b128 v[46:49], v70 offset:34848
	v_lshl_or_b32 v32, v222, 12, v32
	v_add_u32_e32 v78, 0x18800, v32
	v_div_scale_f32 v82, s[0:1], s10, s10, 1.0
	v_rcp_f32_e32 v84, v82
	v_div_scale_f32 v83, vcc, 1.0, s10, 1.0
	s_waitcnt vmcnt(0) lgkmcnt(2)
	v_mfma_f32_32x32x16_f16 v[16:31], v[34:37], v[38:41], v[16:31]
	ds_read_b128 v[34:37], v54 offset:64
	ds_read_b128 v[38:41], v70 offset:34880
	s_waitcnt lgkmcnt(2)
	v_mfma_f32_32x32x16_f16 v[16:31], v[42:45], v[46:49], v[16:31]
	ds_read_b128 v[42:45], v54 offset:96
	ds_read_b128 v[46:49], v70 offset:34912
	s_waitcnt lgkmcnt(2)
	v_mfma_f32_32x32x16_f16 v[16:31], v[34:37], v[38:41], v[16:31]
	ds_read_b128 v[32:35], v54 offset:128
	ds_read_b128 v[36:39], v54 offset:160
	ds_read_b128 v[50:53], v54 offset:192
	ds_read_b128 v[54:57], v54 offset:224
	ds_read_b128 v[58:61], v70 offset:34944
	ds_read_b128 v[62:65], v70 offset:34976
	ds_read_b128 v[66:69], v70 offset:35008
	ds_read_b128 v[70:73], v70 offset:35040
	s_waitcnt lgkmcnt(8)
	v_mfma_f32_32x32x16_f16 v[16:31], v[42:45], v[46:49], v[16:31]
	ds_read_b128 v[40:43], v78
	ds_read_b128 v[44:47], v78 offset:16
	ds_read_b128 v[74:77], v78 offset:32
	ds_read_b128 v[78:81], v78 offset:48
	v_fma_f32 v48, -v82, v84, 1.0
	v_fmac_f32_e32 v84, v48, v84
	v_mul_f32_e32 v48, v83, v84
	s_waitcnt lgkmcnt(7)
	v_mfma_f32_32x32x16_f16 v[16:31], v[32:35], v[58:61], v[16:31]
	s_waitcnt lgkmcnt(3)
	v_add_f32_e64 v32, v0, v40
	v_add_f32_e64 v33, v1, v41
	v_add_f32_e64 v0, v42, v2
	v_add_f32_e64 v1, v43, v3
	s_waitcnt lgkmcnt(2)
	v_pk_add_f32 v[2:3], v[4:5], v[44:45]
	v_pk_add_f32 v[4:5], v[46:47], v[6:7]
	s_waitcnt lgkmcnt(1)
	v_pk_add_f32 v[6:7], v[8:9], v[74:75]
	s_waitcnt lgkmcnt(0)
	v_pk_add_f32 v[8:9], v[12:13], v[78:79]
	v_fma_f32 v12, -v82, v48, v83
	v_mfma_f32_32x32x16_f16 v[16:31], v[36:39], v[62:65], v[16:31]
	v_fmac_f32_e32 v48, v12, v84
	v_cvt_pk_f16_f32 v2, v2, v3
	v_cvt_pk_f16_f32 v3, v4, v5
	v_cvt_pk_f16_f32 v1, v0, v1
	v_cvt_pk_f16_f32 v0, v32, v33
	v_fma_f32 v4, -v82, v48, v83
	v_div_fmas_f32 v4, v4, v84, v48
	v_mfma_f32_32x32x16_f16 v[16:31], v[50:53], v[66:69], v[16:31]
	v_add_f32_e64 v40, v76, v10
	v_add_f32_e64 v41, v77, v11
	v_add_f32_e64 v10, v80, v14
	v_add_f32_e64 v11, v81, v15
	v_div_fixup_f32 v4, v4, s10, 1.0
	v_cvt_pk_f16_f32 v34, v8, v9
	v_cvt_pk_f16_f32 v32, v6, v7
	v_cvt_pk_f16_f32 v35, v10, v11
	v_cvt_pk_f16_f32 v33, v40, v41
	v_mfma_f32_32x32x16_f16 v[16:31], v[54:57], v[70:73], v[16:31]
	s_andn2_b64 vcc, exec, s[8:9]
	s_nop 10
	v_mul_f32_e32 v8, v4, v16
	v_mul_f32_e32 v9, v4, v17
	v_mul_f32_e32 v5, v4, v18
	v_mul_f32_e32 v10, v4, v19
	v_mul_f32_e32 v6, v4, v20
	v_mul_f32_e32 v11, v4, v21
	v_mul_f32_e32 v7, v4, v22
	v_mul_f32_e32 v12, v4, v23
	v_mul_f32_e32 v16, v4, v24
	v_mul_f32_e32 v20, v4, v25
	v_mul_f32_e32 v17, v4, v26
	v_mul_f32_e32 v21, v4, v27
	v_mul_f32_e32 v18, v4, v28
	v_mul_f32_e32 v22, v4, v29
	v_mul_f32_e32 v19, v4, v30
	v_mul_f32_e32 v23, v4, v31
	v_cvt_pk_f16_f32 v7, v7, v12
	v_cvt_pk_f16_f32 v6, v6, v11
	v_cvt_pk_f16_f32 v5, v5, v10
	v_cvt_pk_f16_f32 v4, v8, v9
	v_cvt_pk_f16_f32 v19, v19, v23
	v_cvt_pk_f16_f32 v18, v18, v22
	v_mfma_f32_32x32x16_f16 v[0:15], v[0:3], v[4:7], 0
	v_cvt_pk_f16_f32 v17, v17, v21
	v_cvt_pk_f16_f32 v16, v16, v20
	s_nop 1
	v_mfma_f32_32x32x16_f16 v[0:15], v[32:35], v[16:19], v[0:15]
	s_cbranch_vccnz .LBB0_48
	v_lshlrev_b32_e32 v16, 7, v220
	v_lshl_or_b32 v16, v222, 12, v16
	v_mov_b32_e32 v17, v215
	s_add_i32 s33, s33, s46
	v_lshlrev_b32_e32 v22, 2, v214
	v_lshl_add_u64 v[16:17], v[16:17], 2, s[44:45]
	v_add_u32_e32 v18, s33, v214
	s_mov_b64 s[0:1], 0
	s_movk_i32 s10, 0x3fd
	v_mov_b32_e32 v23, v215
	s_branch .LBB0_43

.LBB0_49:
	s_or_b64 exec, exec, s[6:7]
	s_waitcnt vmcnt(0) lgkmcnt(0)
	s_barrier
	s_and_saveexec_b64 s[0:1], s[4:5]
	s_cbranch_execz .LBB0_51
	v_lshl_or_b32 v0, v219, 5, v220
	v_mul_u32_u24_e32 v0, 0x110, v0
	v_or_b32_e32 v0, v0, v221
	v_add_u32_e32 v28, 0x10000, v0
	v_lshlrev_b32_e32 v29, 4, v218
	ds_read2_b64 v[16:19], v28 offset1:2
	ds_read_b128 v[48:51], v29 offset:43520
	ds_read2_b64 v[20:23], v28 offset0:4 offset1:6
	ds_read_b128 v[52:55], v29 offset:44544
	ds_read2_b64 v[24:27], v28 offset0:8 offset1:10
	ds_read_b128 v[56:59], v29 offset:45568
	ds_read2_b64 v[32:35], v28 offset0:12 offset1:14
	ds_read_b128 v[60:63], v29 offset:46592
	ds_read2_b64 v[36:39], v28 offset0:16 offset1:18
	ds_read_b128 v[64:67], v29 offset:47616
	ds_read2_b64 v[40:43], v28 offset0:20 offset1:22
	ds_read_b128 v[68:71], v29 offset:48640
	ds_read2_b64 v[44:47], v28 offset0:24 offset1:26
	ds_read_b128 v[72:75], v29 offset:49664
	ds_read2_b64 v[76:79], v28 offset0:28 offset1:30
	ds_read_b128 v[80:83], v29 offset:50688
	s_waitcnt lgkmcnt(14)
	v_mfma_f32_32x32x16_f16 v[0:15], v[16:19], v[48:51], 0
	s_waitcnt lgkmcnt(12)
	v_mfma_f32_32x32x16_f16 v[0:15], v[20:23], v[52:55], v[0:15]
	s_waitcnt lgkmcnt(10)
	v_mfma_f32_32x32x16_f16 v[0:15], v[24:27], v[56:59], v[0:15]
	s_waitcnt lgkmcnt(8)
	v_mfma_f32_32x32x16_f16 v[0:15], v[32:35], v[60:63], v[0:15]
	s_waitcnt lgkmcnt(6)
	v_mfma_f32_32x32x16_f16 v[0:15], v[36:39], v[64:67], v[0:15]
	s_waitcnt lgkmcnt(4)
	v_mfma_f32_32x32x16_f16 v[0:15], v[40:43], v[68:71], v[0:15]
	s_waitcnt lgkmcnt(2)
	v_mfma_f32_32x32x16_f16 v[0:15], v[44:47], v[72:75], v[0:15]
	v_lshl_add_u64 v[20:21], v[212:213], 4, s[34:35]
	s_waitcnt lgkmcnt(0)
	v_mfma_f32_32x32x16_f16 v[0:15], v[76:79], v[80:83], v[0:15]
	s_nop 11
	v_cvt_pk_f16_f32 v7, v6, v7
	v_cvt_pk_f16_f32 v6, v4, v5
	v_cvt_pk_f16_f32 v5, v2, v3
	v_cvt_pk_f16_f32 v4, v0, v1
	v_cvt_pk_f16_f32 v3, v14, v15
	v_cvt_pk_f16_f32 v2, v12, v13
	v_cvt_pk_f16_f32 v1, v10, v11
	v_cvt_pk_f16_f32 v0, v8, v9
	global_store_dwordx4 v[20:21], v[4:7], off
	global_store_dwordx4 v[20:21], v[0:3], off offset:16
